# P6 out-projection epilogue software-pipelined: x loads 3 row-blocks ahead, batched sum-of-squares shuffles
# speedup vs baseline: 1.0313x; 1.0063x over previous
.LBB0_1092:
	v_readlane_b32 s48, v252, 23
	v_readlane_b32 s49, v252, 24
	v_readlane_b32 s50, v252, 25
	v_readlane_b32 s51, v252, 26
	v_readlane_b32 s52, v252, 27
	v_readlane_b32 s53, v252, 28
	v_readlane_b32 s54, v252, 29
	v_readlane_b32 s55, v252, 30
	v_readlane_b32 s56, v252, 31
	v_readlane_b32 s57, v252, 32
	v_readlane_b32 s58, v252, 33
	v_readlane_b32 s59, v252, 34
	v_readlane_b32 s60, v252, 35
	v_readlane_b32 s61, v252, 36
	v_readlane_b32 s62, v252, 37
	v_readlane_b32 s63, v252, 38
	v_lshl_add_u32 v152, s10, 8, v1
	v_lshl_or_b32 v150, s64, 8, v155
	s_lshl_b32 s26, s64, 4
	s_lshl_b32 s10, s42, 2
	s_add_i32 s26, s26, s10
	v_lshlrev_b32_e32 v151, 13, v152
	v_lshl_add_u32 v151, v150, 2, v151
	v_lshlrev_b32_e32 v153, 12, v152
	v_lshl_add_u32 v153, v150, 1, v153
	v_lshl_add_u32 v216, v152, 7, s26
	v_xor_b32_e32 v219, 16, v159
	v_lshlrev_b32_e32 v219, 2, v219
	global_load_dwordx4 v[160:163], v151, s[48:49] nt
	global_load_dwordx4 v[164:167], v151, s[48:49] offset:16 nt
	global_load_dwordx4 v[168:171], v151, s[48:49] offset:512 nt
	global_load_dwordx4 v[172:175], v151, s[48:49] offset:528 nt
	v_add_u32_e32 v217, 0x20000, v151
	global_load_dwordx4 v[176:179], v217, s[48:49] nt
	global_load_dwordx4 v[180:183], v217, s[48:49] offset:16 nt
	global_load_dwordx4 v[184:187], v217, s[48:49] offset:512 nt
	global_load_dwordx4 v[188:191], v217, s[48:49] offset:528 nt
	v_add_u32_e32 v217, 0x40000, v151
	global_load_dwordx4 v[192:195], v217, s[48:49] nt
	global_load_dwordx4 v[196:199], v217, s[48:49] offset:16 nt
	global_load_dwordx4 v[200:203], v217, s[48:49] offset:512 nt
	global_load_dwordx4 v[204:207], v217, s[48:49] offset:528 nt
	v_xor_b32_e32 v150, 32, v159
	v_lshlrev_b32_e32 v150, 2, v150
	s_waitcnt vmcnt(8)
	v_pk_add_f32 v[126:127], v[126:127], v[160:161]
	v_pk_add_f32 v[128:129], v[128:129], v[162:163]
	v_pk_add_f32 v[122:123], v[122:123], v[164:165]
	v_pk_add_f32 v[124:125], v[124:125], v[166:167]
	v_pk_add_f32 v[118:119], v[118:119], v[168:169]
	v_pk_add_f32 v[120:121], v[120:121], v[170:171]
	v_pk_add_f32 v[114:115], v[114:115], v[172:173]
	v_pk_add_f32 v[116:117], v[116:117], v[174:175]
	v_cvt_pk_bf16_f32 v208, v126, v127
	v_cvt_pk_bf16_f32 v209, v128, v129
	v_cvt_pk_bf16_f32 v210, v122, v123
	v_cvt_pk_bf16_f32 v211, v124, v125
	global_store_dwordx4 v153, v[208:211], s[0:1]
	v_cvt_pk_bf16_f32 v212, v118, v119
	v_cvt_pk_bf16_f32 v213, v120, v121
	v_cvt_pk_bf16_f32 v214, v114, v115
	v_cvt_pk_bf16_f32 v215, v116, v117
	global_store_dwordx4 v153, v[212:215], s[0:1] offset:256
	v_add_u32_e32 v217, 0x60000, v151
	global_load_dwordx4 v[160:163], v217, s[48:49] nt
	global_load_dwordx4 v[164:167], v217, s[48:49] offset:16 nt
	global_load_dwordx4 v[168:171], v217, s[48:49] offset:512 nt
	global_load_dwordx4 v[172:175], v217, s[48:49] offset:528 nt
	v_mul_f32_e32 v127, v127, v127
	v_mul_f32_e32 v129, v129, v129
	v_fmac_f32_e32 v127, v126, v126
	v_fmac_f32_e32 v129, v128, v128
	v_mul_f32_e32 v123, v123, v123
	v_mul_f32_e32 v125, v125, v125
	v_fmac_f32_e32 v123, v122, v122
	v_fmac_f32_e32 v125, v124, v124
	v_mul_f32_e32 v119, v119, v119
	v_mul_f32_e32 v121, v121, v121
	v_fmac_f32_e32 v119, v118, v118
	v_fmac_f32_e32 v121, v120, v120
	v_mul_f32_e32 v115, v115, v115
	v_mul_f32_e32 v117, v117, v117
	v_fmac_f32_e32 v115, v114, v114
	v_fmac_f32_e32 v117, v116, v116
	v_add_f32_e32 v127, v127, v129
	v_add_f32_e32 v127, v127, v123
	v_add_f32_e32 v127, v125, v127
	v_add_f32_e32 v119, v119, v121
	v_add_f32_e32 v119, v119, v115
	v_add_f32_e32 v119, v117, v119
	v_add_f32_e32 v127, v127, v119
	s_waitcnt vmcnt(10)
	v_pk_add_f32 v[110:111], v[110:111], v[176:177]
	v_pk_add_f32 v[112:113], v[112:113], v[178:179]
	v_pk_add_f32 v[106:107], v[106:107], v[180:181]
	v_pk_add_f32 v[108:109], v[108:109], v[182:183]
	v_pk_add_f32 v[102:103], v[102:103], v[184:185]
	v_pk_add_f32 v[104:105], v[104:105], v[186:187]
	v_pk_add_f32 v[98:99], v[98:99], v[188:189]
	v_pk_add_f32 v[100:101], v[100:101], v[190:191]
	v_add_u32_e32 v218, 0x10000, v153
	v_cvt_pk_bf16_f32 v208, v110, v111
	v_cvt_pk_bf16_f32 v209, v112, v113
	v_cvt_pk_bf16_f32 v210, v106, v107
	v_cvt_pk_bf16_f32 v211, v108, v109
	global_store_dwordx4 v218, v[208:211], s[0:1]
	v_cvt_pk_bf16_f32 v212, v102, v103
	v_cvt_pk_bf16_f32 v213, v104, v105
	v_cvt_pk_bf16_f32 v214, v98, v99
	v_cvt_pk_bf16_f32 v215, v100, v101
	global_store_dwordx4 v218, v[212:215], s[0:1] offset:256
	v_add_u32_e32 v217, 0x100000, v151
	global_load_dwordx4 v[176:179], v217, s[48:49] nt
	global_load_dwordx4 v[180:183], v217, s[48:49] offset:16 nt
	global_load_dwordx4 v[184:187], v217, s[48:49] offset:512 nt
	global_load_dwordx4 v[188:191], v217, s[48:49] offset:528 nt
	v_mul_f32_e32 v111, v111, v111
	v_mul_f32_e32 v113, v113, v113
	v_fmac_f32_e32 v111, v110, v110
	v_fmac_f32_e32 v113, v112, v112
	v_mul_f32_e32 v107, v107, v107
	v_mul_f32_e32 v109, v109, v109
	v_fmac_f32_e32 v107, v106, v106
	v_fmac_f32_e32 v109, v108, v108
	v_mul_f32_e32 v103, v103, v103
	v_mul_f32_e32 v105, v105, v105
	v_fmac_f32_e32 v103, v102, v102
	v_fmac_f32_e32 v105, v104, v104
	v_mul_f32_e32 v99, v99, v99
	v_mul_f32_e32 v101, v101, v101
	v_fmac_f32_e32 v99, v98, v98
	v_fmac_f32_e32 v101, v100, v100
	v_add_f32_e32 v111, v111, v113
	v_add_f32_e32 v111, v111, v107
	v_add_f32_e32 v111, v109, v111
	v_add_f32_e32 v103, v103, v105
	v_add_f32_e32 v103, v103, v99
	v_add_f32_e32 v103, v101, v103
	v_add_f32_e32 v111, v111, v103
	s_waitcnt vmcnt(12)
	v_pk_add_f32 v[94:95], v[94:95], v[192:193]
	v_pk_add_f32 v[96:97], v[96:97], v[194:195]
	v_pk_add_f32 v[90:91], v[90:91], v[196:197]
	v_pk_add_f32 v[92:93], v[92:93], v[198:199]
	v_pk_add_f32 v[86:87], v[86:87], v[200:201]
	v_pk_add_f32 v[88:89], v[88:89], v[202:203]
	v_pk_add_f32 v[82:83], v[82:83], v[204:205]
	v_pk_add_f32 v[84:85], v[84:85], v[206:207]
	v_add_u32_e32 v218, 0x20000, v153
	v_cvt_pk_bf16_f32 v208, v94, v95
	v_cvt_pk_bf16_f32 v209, v96, v97
	v_cvt_pk_bf16_f32 v210, v90, v91
	v_cvt_pk_bf16_f32 v211, v92, v93
	global_store_dwordx4 v218, v[208:211], s[0:1]
	v_cvt_pk_bf16_f32 v212, v86, v87
	v_cvt_pk_bf16_f32 v213, v88, v89
	v_cvt_pk_bf16_f32 v214, v82, v83
	v_cvt_pk_bf16_f32 v215, v84, v85
	global_store_dwordx4 v218, v[212:215], s[0:1] offset:256
	v_add_u32_e32 v217, 0x120000, v151
	global_load_dwordx4 v[192:195], v217, s[48:49] nt
	global_load_dwordx4 v[196:199], v217, s[48:49] offset:16 nt
	global_load_dwordx4 v[200:203], v217, s[48:49] offset:512 nt
	global_load_dwordx4 v[204:207], v217, s[48:49] offset:528 nt
	v_mul_f32_e32 v95, v95, v95
	v_mul_f32_e32 v97, v97, v97
	v_fmac_f32_e32 v95, v94, v94
	v_fmac_f32_e32 v97, v96, v96
	v_mul_f32_e32 v91, v91, v91
	v_mul_f32_e32 v93, v93, v93
	v_fmac_f32_e32 v91, v90, v90
	v_fmac_f32_e32 v93, v92, v92
	v_mul_f32_e32 v87, v87, v87
	v_mul_f32_e32 v89, v89, v89
	v_fmac_f32_e32 v87, v86, v86
	v_fmac_f32_e32 v89, v88, v88
	v_mul_f32_e32 v83, v83, v83
	v_mul_f32_e32 v85, v85, v85
	v_fmac_f32_e32 v83, v82, v82
	v_fmac_f32_e32 v85, v84, v84
	v_add_f32_e32 v95, v95, v97
	v_add_f32_e32 v95, v95, v91
	v_add_f32_e32 v95, v93, v95
	v_add_f32_e32 v87, v87, v89
	v_add_f32_e32 v87, v87, v83
	v_add_f32_e32 v87, v85, v87
	v_add_f32_e32 v95, v95, v87
	s_waitcnt vmcnt(12)
	v_pk_add_f32 v[78:79], v[78:79], v[160:161]
	v_pk_add_f32 v[80:81], v[80:81], v[162:163]
	v_pk_add_f32 v[74:75], v[74:75], v[164:165]
	v_pk_add_f32 v[76:77], v[76:77], v[166:167]
	v_pk_add_f32 v[70:71], v[70:71], v[168:169]
	v_pk_add_f32 v[72:73], v[72:73], v[170:171]
	v_pk_add_f32 v[66:67], v[66:67], v[172:173]
	v_pk_add_f32 v[68:69], v[68:69], v[174:175]
	v_add_u32_e32 v218, 0x30000, v153
	v_cvt_pk_bf16_f32 v208, v78, v79
	v_cvt_pk_bf16_f32 v209, v80, v81
	v_cvt_pk_bf16_f32 v210, v74, v75
	v_cvt_pk_bf16_f32 v211, v76, v77
	global_store_dwordx4 v218, v[208:211], s[0:1]
	v_cvt_pk_bf16_f32 v212, v70, v71
	v_cvt_pk_bf16_f32 v213, v72, v73
	v_cvt_pk_bf16_f32 v214, v66, v67
	v_cvt_pk_bf16_f32 v215, v68, v69
	global_store_dwordx4 v218, v[212:215], s[0:1] offset:256
	v_add_u32_e32 v217, 0x140000, v151
	global_load_dwordx4 v[160:163], v217, s[48:49] nt
	global_load_dwordx4 v[164:167], v217, s[48:49] offset:16 nt
	global_load_dwordx4 v[168:171], v217, s[48:49] offset:512 nt
	global_load_dwordx4 v[172:175], v217, s[48:49] offset:528 nt
	v_mul_f32_e32 v79, v79, v79
	v_mul_f32_e32 v81, v81, v81
	v_fmac_f32_e32 v79, v78, v78
	v_fmac_f32_e32 v81, v80, v80
	v_mul_f32_e32 v75, v75, v75
	v_mul_f32_e32 v77, v77, v77
	v_fmac_f32_e32 v75, v74, v74
	v_fmac_f32_e32 v77, v76, v76
	v_mul_f32_e32 v71, v71, v71
	v_mul_f32_e32 v73, v73, v73
	v_fmac_f32_e32 v71, v70, v70
	v_fmac_f32_e32 v73, v72, v72
	v_mul_f32_e32 v67, v67, v67
	v_mul_f32_e32 v69, v69, v69
	v_fmac_f32_e32 v67, v66, v66
	v_fmac_f32_e32 v69, v68, v68
	v_add_f32_e32 v79, v79, v81
	v_add_f32_e32 v79, v79, v75
	v_add_f32_e32 v79, v77, v79
	v_add_f32_e32 v71, v71, v73
	v_add_f32_e32 v71, v71, v67
	v_add_f32_e32 v71, v69, v71
	v_add_f32_e32 v79, v79, v71
	s_waitcnt vmcnt(12)
	v_pk_add_f32 v[54:55], v[54:55], v[176:177]
	v_pk_add_f32 v[56:57], v[56:57], v[178:179]
	v_pk_add_f32 v[50:51], v[50:51], v[180:181]
	v_pk_add_f32 v[52:53], v[52:53], v[182:183]
	v_pk_add_f32 v[62:63], v[62:63], v[184:185]
	v_pk_add_f32 v[64:65], v[64:65], v[186:187]
	v_pk_add_f32 v[58:59], v[58:59], v[188:189]
	v_pk_add_f32 v[60:61], v[60:61], v[190:191]
	v_add_u32_e32 v218, 0x80000, v153
	v_cvt_pk_bf16_f32 v208, v54, v55
	v_cvt_pk_bf16_f32 v209, v56, v57
	v_cvt_pk_bf16_f32 v210, v50, v51
	v_cvt_pk_bf16_f32 v211, v52, v53
	global_store_dwordx4 v218, v[208:211], s[0:1]
	v_cvt_pk_bf16_f32 v212, v62, v63
	v_cvt_pk_bf16_f32 v213, v64, v65
	v_cvt_pk_bf16_f32 v214, v58, v59
	v_cvt_pk_bf16_f32 v215, v60, v61
	global_store_dwordx4 v218, v[212:215], s[0:1] offset:256
	v_add_u32_e32 v217, 0x160000, v151
	global_load_dwordx4 v[176:179], v217, s[48:49] nt
	global_load_dwordx4 v[180:183], v217, s[48:49] offset:16 nt
	global_load_dwordx4 v[184:187], v217, s[48:49] offset:512 nt
	global_load_dwordx4 v[188:191], v217, s[48:49] offset:528 nt
	v_mul_f32_e32 v55, v55, v55
	v_mul_f32_e32 v57, v57, v57
	v_fmac_f32_e32 v55, v54, v54
	v_fmac_f32_e32 v57, v56, v56
	v_mul_f32_e32 v51, v51, v51
	v_mul_f32_e32 v53, v53, v53
	v_fmac_f32_e32 v51, v50, v50
	v_fmac_f32_e32 v53, v52, v52
	v_mul_f32_e32 v63, v63, v63
	v_mul_f32_e32 v65, v65, v65
	v_fmac_f32_e32 v63, v62, v62
	v_fmac_f32_e32 v65, v64, v64
	v_mul_f32_e32 v59, v59, v59
	v_mul_f32_e32 v61, v61, v61
	v_fmac_f32_e32 v59, v58, v58
	v_fmac_f32_e32 v61, v60, v60
	v_add_f32_e32 v55, v55, v57
	v_add_f32_e32 v55, v55, v51
	v_add_f32_e32 v55, v53, v55
	v_add_f32_e32 v63, v63, v65
	v_add_f32_e32 v63, v63, v59
	v_add_f32_e32 v63, v61, v63
	v_add_f32_e32 v55, v55, v63
	s_waitcnt vmcnt(12)
	v_pk_add_f32 v[38:39], v[38:39], v[192:193]
	v_pk_add_f32 v[40:41], v[40:41], v[194:195]
	v_pk_add_f32 v[34:35], v[34:35], v[196:197]
	v_pk_add_f32 v[36:37], v[36:37], v[198:199]
	v_pk_add_f32 v[46:47], v[46:47], v[200:201]
	v_pk_add_f32 v[48:49], v[48:49], v[202:203]
	v_pk_add_f32 v[42:43], v[42:43], v[204:205]
	v_pk_add_f32 v[44:45], v[44:45], v[206:207]
	v_add_u32_e32 v218, 0x90000, v153
	v_cvt_pk_bf16_f32 v208, v38, v39
	v_cvt_pk_bf16_f32 v209, v40, v41
	v_cvt_pk_bf16_f32 v210, v34, v35
	v_cvt_pk_bf16_f32 v211, v36, v37
	global_store_dwordx4 v218, v[208:211], s[0:1]
	v_cvt_pk_bf16_f32 v212, v46, v47
	v_cvt_pk_bf16_f32 v213, v48, v49
	v_cvt_pk_bf16_f32 v214, v42, v43
	v_cvt_pk_bf16_f32 v215, v44, v45
	global_store_dwordx4 v218, v[212:215], s[0:1] offset:256
	v_mul_f32_e32 v39, v39, v39
	v_mul_f32_e32 v41, v41, v41
	v_fmac_f32_e32 v39, v38, v38
	v_fmac_f32_e32 v41, v40, v40
	v_mul_f32_e32 v35, v35, v35
	v_mul_f32_e32 v37, v37, v37
	v_fmac_f32_e32 v35, v34, v34
	v_fmac_f32_e32 v37, v36, v36
	v_mul_f32_e32 v47, v47, v47
	v_mul_f32_e32 v49, v49, v49
	v_fmac_f32_e32 v47, v46, v46
	v_fmac_f32_e32 v49, v48, v48
	v_mul_f32_e32 v43, v43, v43
	v_mul_f32_e32 v45, v45, v45
	v_fmac_f32_e32 v43, v42, v42
	v_fmac_f32_e32 v45, v44, v44
	v_add_f32_e32 v39, v39, v41
	v_add_f32_e32 v39, v39, v35
	v_add_f32_e32 v39, v37, v39
	v_add_f32_e32 v47, v47, v49
	v_add_f32_e32 v47, v47, v43
	v_add_f32_e32 v47, v45, v47
	v_add_f32_e32 v39, v39, v47
	s_waitcnt vmcnt(8)
	v_pk_add_f32 v[22:23], v[22:23], v[160:161]
	v_pk_add_f32 v[24:25], v[24:25], v[162:163]
	v_pk_add_f32 v[18:19], v[18:19], v[164:165]
	v_pk_add_f32 v[20:21], v[20:21], v[166:167]
	v_pk_add_f32 v[30:31], v[30:31], v[168:169]
	v_pk_add_f32 v[32:33], v[32:33], v[170:171]
	v_pk_add_f32 v[26:27], v[26:27], v[172:173]
	v_pk_add_f32 v[28:29], v[28:29], v[174:175]
	v_add_u32_e32 v218, 0xa0000, v153
	v_cvt_pk_bf16_f32 v208, v22, v23
	v_cvt_pk_bf16_f32 v209, v24, v25
	v_cvt_pk_bf16_f32 v210, v18, v19
	v_cvt_pk_bf16_f32 v211, v20, v21
	global_store_dwordx4 v218, v[208:211], s[0:1]
	v_cvt_pk_bf16_f32 v212, v30, v31
	v_cvt_pk_bf16_f32 v213, v32, v33
	v_cvt_pk_bf16_f32 v214, v26, v27
	v_cvt_pk_bf16_f32 v215, v28, v29
	global_store_dwordx4 v218, v[212:215], s[0:1] offset:256
	v_mul_f32_e32 v23, v23, v23
	v_mul_f32_e32 v25, v25, v25
	v_fmac_f32_e32 v23, v22, v22
	v_fmac_f32_e32 v25, v24, v24
	v_mul_f32_e32 v19, v19, v19
	v_mul_f32_e32 v21, v21, v21
	v_fmac_f32_e32 v19, v18, v18
	v_fmac_f32_e32 v21, v20, v20
	v_mul_f32_e32 v31, v31, v31
	v_mul_f32_e32 v33, v33, v33
	v_fmac_f32_e32 v31, v30, v30
	v_fmac_f32_e32 v33, v32, v32
	v_mul_f32_e32 v27, v27, v27
	v_mul_f32_e32 v29, v29, v29
	v_fmac_f32_e32 v27, v26, v26
	v_fmac_f32_e32 v29, v28, v28
	v_add_f32_e32 v23, v23, v25
	v_add_f32_e32 v23, v23, v19
	v_add_f32_e32 v23, v21, v23
	v_add_f32_e32 v31, v31, v33
	v_add_f32_e32 v31, v31, v27
	v_add_f32_e32 v31, v29, v31
	v_add_f32_e32 v23, v23, v31
	s_waitcnt vmcnt(4)
	v_pk_add_f32 v[6:7], v[6:7], v[176:177]
	v_pk_add_f32 v[8:9], v[8:9], v[178:179]
	v_pk_add_f32 v[2:3], v[2:3], v[180:181]
	v_pk_add_f32 v[4:5], v[4:5], v[182:183]
	v_pk_add_f32 v[14:15], v[14:15], v[184:185]
	v_pk_add_f32 v[16:17], v[16:17], v[186:187]
	v_pk_add_f32 v[10:11], v[10:11], v[188:189]
	v_pk_add_f32 v[12:13], v[12:13], v[190:191]
	v_add_u32_e32 v218, 0xb0000, v153
	v_cvt_pk_bf16_f32 v208, v6, v7
	v_cvt_pk_bf16_f32 v209, v8, v9
	v_cvt_pk_bf16_f32 v210, v2, v3
	v_cvt_pk_bf16_f32 v211, v4, v5
	global_store_dwordx4 v218, v[208:211], s[0:1]
	v_cvt_pk_bf16_f32 v212, v14, v15
	v_cvt_pk_bf16_f32 v213, v16, v17
	v_cvt_pk_bf16_f32 v214, v10, v11
	v_cvt_pk_bf16_f32 v215, v12, v13
	global_store_dwordx4 v218, v[212:215], s[0:1] offset:256
	v_mul_f32_e32 v7, v7, v7
	v_mul_f32_e32 v9, v9, v9
	v_fmac_f32_e32 v7, v6, v6
	v_fmac_f32_e32 v9, v8, v8
	v_mul_f32_e32 v3, v3, v3
	v_mul_f32_e32 v5, v5, v5
	v_fmac_f32_e32 v3, v2, v2
	v_fmac_f32_e32 v5, v4, v4
	v_mul_f32_e32 v15, v15, v15
	v_mul_f32_e32 v17, v17, v17
	v_fmac_f32_e32 v15, v14, v14
	v_fmac_f32_e32 v17, v16, v16
	v_mul_f32_e32 v11, v11, v11
	v_mul_f32_e32 v13, v13, v13
	v_fmac_f32_e32 v11, v10, v10
	v_fmac_f32_e32 v13, v12, v12
	v_add_f32_e32 v7, v7, v9
	v_add_f32_e32 v7, v7, v3
	v_add_f32_e32 v7, v5, v7
	v_add_f32_e32 v15, v15, v17
	v_add_f32_e32 v15, v15, v11
	v_add_f32_e32 v15, v13, v15
	v_add_f32_e32 v7, v7, v15
	ds_bpermute_b32 v126, v219, v127
	ds_bpermute_b32 v110, v219, v111
	ds_bpermute_b32 v94, v219, v95
	ds_bpermute_b32 v78, v219, v79
	ds_bpermute_b32 v54, v219, v55
	ds_bpermute_b32 v38, v219, v39
	ds_bpermute_b32 v22, v219, v23
	ds_bpermute_b32 v6, v219, v7
	s_waitcnt lgkmcnt(7)
	v_add_f32_e32 v127, v127, v126
	s_waitcnt lgkmcnt(6)
	v_add_f32_e32 v111, v111, v110
	s_waitcnt lgkmcnt(5)
	v_add_f32_e32 v95, v95, v94
	s_waitcnt lgkmcnt(4)
	v_add_f32_e32 v79, v79, v78
	s_waitcnt lgkmcnt(3)
	v_add_f32_e32 v55, v55, v54
	s_waitcnt lgkmcnt(2)
	v_add_f32_e32 v39, v39, v38
	s_waitcnt lgkmcnt(1)
	v_add_f32_e32 v23, v23, v22
	s_waitcnt lgkmcnt(0)
	v_add_f32_e32 v7, v7, v6
	ds_bpermute_b32 v126, v150, v127
	ds_bpermute_b32 v110, v150, v111
	ds_bpermute_b32 v94, v150, v95
	ds_bpermute_b32 v78, v150, v79
	ds_bpermute_b32 v54, v150, v55
	ds_bpermute_b32 v38, v150, v39
	ds_bpermute_b32 v22, v150, v23
	ds_bpermute_b32 v6, v150, v7
	s_waitcnt lgkmcnt(7)
	v_add_f32_e32 v127, v127, v126
	s_waitcnt lgkmcnt(6)
	v_add_f32_e32 v111, v111, v110
	s_waitcnt lgkmcnt(5)
	v_add_f32_e32 v95, v95, v94
	s_waitcnt lgkmcnt(4)
	v_add_f32_e32 v79, v79, v78
	s_waitcnt lgkmcnt(3)
	v_add_f32_e32 v55, v55, v54
	s_waitcnt lgkmcnt(2)
	v_add_f32_e32 v39, v39, v38
	s_waitcnt lgkmcnt(1)
	v_add_f32_e32 v23, v23, v22
	s_waitcnt lgkmcnt(0)
	v_add_f32_e32 v7, v7, v6
	s_and_saveexec_b64 s[28:29], s[4:5]
	global_store_dword v216, v127, s[6:7]
	v_add_u32_e32 v110, 0x800, v216
	global_store_dword v110, v111, s[6:7]
	v_add_u32_e32 v94, 0x1000, v216
	global_store_dword v94, v95, s[6:7]
	v_add_u32_e32 v78, 0x1800, v216
	global_store_dword v78, v79, s[6:7]
	v_add_u32_e32 v54, 0x4000, v216
	global_store_dword v54, v55, s[6:7]
	v_add_u32_e32 v38, 0x4800, v216
	global_store_dword v38, v39, s[6:7]
	v_add_u32_e32 v22, 0x5000, v216
	global_store_dword v22, v23, s[6:7]
	v_add_u32_e32 v6, 0x5800, v216
	global_store_dword v6, v7, s[6:7]
